# speedup vs baseline: 1.0327x; 1.0053x over previous
_Z11attn_kernelPK14__hip_bfloat16S1_S1_PS_:
	s_lshr_b32 s3, s2, 3
	s_and_b32 s33, s2, 7
	s_sub_i32 s4, 63, s3
	s_sub_i32 s3, s3, 32
	s_cmpk_lt_u32 s2, 0x100
	s_cselect_b32 s2, s4, s3
	v_lshrrev_b32_e32 v1, 6, v0
	s_ashr_i32 s77, s2, 1
	v_and_b32_e32 v184, 63, v0
	v_bfe_u32 v186, v0, 5, 1
	v_and_b32_e32 v185, 31, v0
	s_lshl_b32 s76, s2, 5
	v_cmp_ge_i32_e32 vcc, s77, v1
	v_mbcnt_lo_u32_b32 v50, -1, 0
	s_and_saveexec_b64 s[4:5], vcc
	s_xor_b64 s[70:71], exec, s[4:5]
	s_cbranch_execz .LBB2_8
	s_load_dwordx4 s[4:7], s[0:1], 0x0
	s_load_dwordx2 s[8:9], s[0:1], 0x10
	s_lshl_b32 s3, s33, 8
	s_lshl_b32 s2, s2, 2
	s_add_i32 s2, s2, s3
	s_ashr_i32 s3, s2, 31
	s_lshl_b64 s[2:3], s[2:3], 10
	s_waitcnt lgkmcnt(0)
	s_add_u32 s2, s4, s2
	s_addc_u32 s3, s5, s3
	s_lshl_b32 s10, s33, 18
	s_add_u32 s4, s6, s10
	s_addc_u32 s5, s7, 0
	s_add_u32 s6, s8, s10
	v_lshlrev_b32_e32 v34, 4, v184
	v_mov_b32_e32 v35, 0
	s_addc_u32 s7, s9, 0
	s_mov_b64 s[80:81], s[4:5]
	s_mov_b64 s[82:83], s[6:7]
	v_lshlrev_b32_e32 v203, 4, v184
	v_readfirstlane_b32 s78, v1
	global_load_dwordx4 v[68:71], v34, s[2:3]
	global_load_dwordx4 v[72:75], v34, s[2:3] offset:1024
	global_load_dwordx4 v[76:79], v34, s[2:3] offset:2048
	global_load_dwordx4 v[80:83], v34, s[2:3] offset:3072
	v_lshl_add_u64 v[180:181], s[4:5], 0, v[34:35]
	v_lshl_add_u64 v[182:183], s[6:7], 0, v[34:35]
	v_lshlrev_b32_e32 v34, 13, v1
	v_lshl_add_u64 v[2:3], v[180:181], 0, v[34:35]
	global_load_dwordx4 v[100:103], v[2:3], off
	global_load_dwordx4 v[108:111], v[2:3], off offset:1024
	global_load_dwordx4 v[116:119], v[2:3], off offset:2048
	global_load_dwordx4 v[120:123], v[2:3], off offset:3072
	v_or_b32_e32 v2, 0x1000, v34
	v_mov_b32_e32 v3, v35
	v_lshl_add_u64 v[4:5], v[180:181], 0, v[2:3]
	v_or_b32_e32 v6, 0x1400, v34
	v_mov_b32_e32 v7, v35
	v_lshl_add_u64 v[8:9], v[180:181], 0, v[6:7]
	global_load_dwordx4 v[132:135], v[4:5], off
	global_load_dwordx4 v[136:139], v[8:9], off
	v_or_b32_e32 v4, 0x1800, v34
	v_mov_b32_e32 v5, v35
	v_lshl_add_u64 v[8:9], v[180:181], 0, v[4:5]
	v_or_b32_e32 v10, 0x1c00, v34
	v_mov_b32_e32 v11, v35
	v_lshl_add_u64 v[12:13], v[180:181], 0, v[10:11]
	global_load_dwordx4 v[140:143], v[8:9], off
	global_load_dwordx4 v[144:147], v[12:13], off
	v_lshl_add_u64 v[8:9], v[182:183], 0, v[34:35]
	global_load_dwordx4 v[128:131], v[8:9], off
	global_load_dwordx4 v[124:127], v[8:9], off offset:1024
	global_load_dwordx4 v[112:115], v[8:9], off offset:2048
	global_load_dwordx4 v[104:107], v[8:9], off offset:3072
	v_lshl_add_u64 v[2:3], v[182:183], 0, v[2:3]
	v_lshl_add_u64 v[6:7], v[182:183], 0, v[6:7]
	global_load_dwordx4 v[84:87], v[2:3], off
	global_load_dwordx4 v[96:99], v[6:7], off
	v_lshl_add_u64 v[2:3], v[182:183], 0, v[4:5]
	v_lshl_add_u64 v[4:5], v[182:183], 0, v[10:11]
	global_load_dwordx4 v[88:91], v[2:3], off
	global_load_dwordx4 v[92:95], v[4:5], off
	v_lshlrev_b32_e32 v2, 2, v186
	v_lshl_or_b32 v2, s77, 6, v2
	v_or_b32_e32 v14, s76, v185
	v_or_b32_e32 v3, 32, v2
	v_cmp_gt_i32_e64 s[4:5], v3, v14
	v_or_b32_e32 v3, 33, v2
	v_cmp_gt_i32_e64 s[8:9], v3, v14
	v_or_b32_e32 v3, 2, v2
	v_cmp_gt_i32_e64 s[10:11], v3, v14
	v_or_b32_e32 v3, 34, v2
	v_cmp_gt_i32_e64 s[12:13], v3, v14
	v_or_b32_e32 v3, 3, v2
	v_cmp_gt_i32_e64 s[14:15], v3, v14
	v_or_b32_e32 v3, 35, v2
	v_cmp_gt_i32_e64 s[16:17], v3, v14
	v_or_b32_e32 v3, 8, v2
	v_cmp_gt_i32_e64 s[18:19], v3, v14
	v_or_b32_e32 v3, 40, v2
	v_cmp_gt_i32_e64 s[20:21], v3, v14
	v_or_b32_e32 v3, 9, v2
	v_cmp_gt_i32_e64 s[22:23], v3, v14
	v_or_b32_e32 v3, 41, v2
	v_cmp_gt_i32_e64 s[24:25], v3, v14
	v_or_b32_e32 v3, 10, v2
	v_cmp_gt_i32_e64 s[26:27], v3, v14
	v_or_b32_e32 v3, 42, v2
	v_cmp_gt_i32_e64 s[28:29], v3, v14
	v_or_b32_e32 v3, 11, v2
	v_cmp_gt_i32_e64 s[30:31], v3, v14
	v_or_b32_e32 v3, 43, v2
	v_cmp_gt_i32_e64 s[34:35], v3, v14
	v_or_b32_e32 v3, 16, v2
	v_cmp_gt_i32_e64 s[36:37], v3, v14
	v_or_b32_e32 v3, 48, v2
	v_cmp_gt_i32_e64 s[38:39], v3, v14
	v_or_b32_e32 v3, 17, v2
	v_cmp_gt_i32_e64 s[40:41], v3, v14
	v_or_b32_e32 v3, 49, v2
	v_cmp_gt_i32_e64 s[42:43], v3, v14
	v_or_b32_e32 v3, 18, v2
	v_cmp_gt_i32_e64 s[44:45], v3, v14
	v_or_b32_e32 v3, 50, v2
	v_cmp_gt_i32_e64 s[46:47], v3, v14
	v_or_b32_e32 v3, 19, v2
	v_cmp_gt_i32_e64 s[48:49], v3, v14
	v_or_b32_e32 v3, 51, v2
	v_cmp_gt_i32_e64 s[50:51], v3, v14
	v_or_b32_e32 v3, 24, v2
	v_cmp_gt_i32_e64 s[52:53], v3, v14
	v_or_b32_e32 v3, 56, v2
	v_cmp_gt_i32_e64 s[54:55], v3, v14
	v_or_b32_e32 v3, 25, v2
	v_cmp_gt_i32_e64 s[56:57], v3, v14
	v_or_b32_e32 v3, 57, v2
	v_cmp_gt_i32_e64 s[58:59], v3, v14
	v_or_b32_e32 v3, 26, v2
	v_cmp_gt_i32_e64 s[60:61], v3, v14
	v_or_b32_e32 v3, 58, v2
	v_cmp_gt_i32_e64 s[2:3], v2, v14
	v_cmp_lt_i32_e64 s[6:7], v2, v14
	v_cmp_gt_i32_e64 s[62:63], v3, v14
	v_or_b32_e32 v3, 27, v2
	v_or_b32_e32 v2, 59, v2
	v_mov_b32_e32 v34, v35
	v_cmp_gt_i32_e64 s[64:65], v3, v14
	v_cmp_gt_i32_e64 s[66:67], v2, v14
	v_mov_b32_e32 v36, v35
	v_mov_b32_e32 v37, v35
	v_mov_b32_e32 v38, v35
	v_mov_b32_e32 v39, v35
	v_mov_b32_e32 v40, v35
	v_mov_b32_e32 v41, v35
	v_mov_b32_e32 v42, v35
	v_mov_b32_e32 v43, v35
	v_mov_b32_e32 v44, v35
	v_mov_b32_e32 v45, v35
	v_mov_b32_e32 v46, v35
	v_mov_b32_e32 v47, v35
	v_mov_b32_e32 v48, v35
	v_mov_b32_e32 v49, v35
	v_mov_b64_e32 v[18:19], v[34:35]
	v_mov_b64_e32 v[2:3], v[34:35]
	v_mov_b32_e32 v190, 0xf149f2ca
	s_mov_b64 s[72:73], 0
	v_mbcnt_hi_u32_b32 v188, -1, v50
	v_mov_b32_e32 v187, 0
	v_mov_b64_e32 v[20:21], v[36:37]
	v_mov_b64_e32 v[22:23], v[38:39]
	v_mov_b64_e32 v[24:25], v[40:41]
	v_mov_b64_e32 v[26:27], v[42:43]
	v_mov_b64_e32 v[28:29], v[44:45]
	v_mov_b64_e32 v[30:31], v[46:47]
	v_mov_b64_e32 v[32:33], v[48:49]
	v_mov_b32_e32 v189, 0xf149f2ca
	v_mov_b32_e32 v191, v1
	v_mov_b64_e32 v[4:5], v[36:37]
	v_mov_b64_e32 v[6:7], v[38:39]
	v_mov_b64_e32 v[8:9], v[40:41]
	v_mov_b64_e32 v[10:11], v[42:43]
	v_mov_b64_e32 v[12:13], v[44:45]
	v_mov_b64_e32 v[14:15], v[46:47]
	v_mov_b64_e32 v[16:17], v[48:49]
	s_branch .LBB2_3

.LBB2_3:
	s_add_u32 s79, s78, 4
	s_cmp_lt_i32 s77, s79
	s_cselect_b32 s79, s78, s79
	s_add_u32 s78, s78, 4
	s_lshl_b32 s79, s79, 13
	s_add_u32 s84, s80, s79
	s_addc_u32 s85, s81, 0
	s_add_u32 s86, s84, 0x1000
	s_addc_u32 s87, s85, 0
	s_add_u32 s88, s82, s79
	s_addc_u32 s89, s83, 0
	s_add_u32 s90, s88, 0x1000
	s_addc_u32 s91, s89, 0
	v_mov_b32_e32 v196, v191
	s_waitcnt vmcnt(9)
	v_mov_b64_e32 v[158:159], v[142:143]
	v_add_u32_e32 v191, 4, v196
	v_mfma_f32_32x32x16_bf16 v[52:67], v[100:103], v[68:71], 0
	v_mov_b64_e32 v[156:157], v[140:141]
	v_mov_b64_e32 v[142:143], v[138:139]
	v_cmp_lt_i32_e64 s[68:69], s77, v191
	v_mov_b64_e32 v[140:141], v[136:137]
	v_mov_b64_e32 v[138:139], v[110:111]
	v_mov_b64_e32 v[136:137], v[108:109]
	global_load_dwordx4 v[100:103], v203, s[84:85]
	global_load_dwordx4 v[108:111], v203, s[84:85] offset:1024
	v_mfma_f32_32x32x16_bf16 v[36:51], v[132:135], v[68:71], 0
	s_waitcnt vmcnt(10)
	v_mov_b64_e32 v[194:195], v[146:147]
	v_mov_b64_e32 v[192:193], v[144:145]
	v_mov_b64_e32 v[146:147], v[118:119]
	v_mov_b64_e32 v[144:145], v[116:117]
	v_mov_b64_e32 v[174:175], v[122:123]
	v_mov_b64_e32 v[172:173], v[120:121]
	v_mfma_f32_32x32x16_bf16 v[52:67], v[136:139], v[72:75], v[52:67]
	v_mfma_f32_32x32x16_bf16 v[36:51], v[140:143], v[72:75], v[36:51]
	v_mfma_f32_32x32x16_bf16 v[52:67], v[144:147], v[76:79], v[52:67]
	global_load_dwordx4 v[116:119], v203, s[84:85] offset:2048
	s_nop 0
	global_load_dwordx4 v[120:123], v203, s[84:85] offset:3072
	s_nop 0
	global_load_dwordx4 v[132:135], v203, s[86:87]
	s_nop 0
	global_load_dwordx4 v[136:139], v203, s[86:87] offset:1024
	s_nop 0
	global_load_dwordx4 v[140:143], v203, s[86:87] offset:2048
	s_nop 0
	global_load_dwordx4 v[144:147], v203, s[86:87] offset:3072
	global_load_dwordx4 v[148:151], v203, s[88:89]
	s_nop 0
	global_load_dwordx4 v[152:155], v203, s[88:89] offset:1024
	v_mfma_f32_32x32x16_bf16 v[36:51], v[156:159], v[76:79], v[36:51]
	global_load_dwordx4 v[156:159], v203, s[88:89] offset:2048
	global_load_dwordx4 v[168:171], v203, s[88:89] offset:3072
	global_load_dwordx4 v[160:163], v203, s[90:91]
	s_nop 0
	global_load_dwordx4 v[164:167], v203, s[90:91] offset:1024
	v_cmp_eq_u32_e32 vcc, s77, v196
	v_mfma_f32_32x32x16_bf16 v[52:67], v[172:175], v[80:83], v[52:67]
	global_load_dwordx4 v[172:175], v203, s[90:91] offset:2048
	s_nop 0
	global_load_dwordx4 v[176:179], v203, s[90:91] offset:3072
	v_mfma_f32_32x32x16_bf16 v[36:51], v[192:195], v[80:83], v[36:51]
	s_and_saveexec_b64 s[74:75], vcc
	s_cbranch_execz .LBB2_5
	s_nop 5
	v_cndmask_b32_e64 v34, v52, v190, s[2:3]
	s_nop 2
	v_cndmask_b32_e64 v36, v36, v190, s[4:5]
	v_cndmask_b32_e64 v53, v190, v53, s[6:7]
	v_cndmask_b32_e64 v52, v34, v52, s[6:7]
	v_cndmask_b32_e64 v37, v37, v190, s[8:9]
	v_cndmask_b32_e64 v54, v54, v190, s[10:11]
	v_cndmask_b32_e64 v38, v38, v190, s[12:13]
	v_cndmask_b32_e64 v55, v55, v190, s[14:15]
	v_cndmask_b32_e64 v39, v39, v190, s[16:17]
	v_cndmask_b32_e64 v56, v56, v190, s[18:19]
	v_cndmask_b32_e64 v40, v40, v190, s[20:21]
	v_cndmask_b32_e64 v57, v57, v190, s[22:23]
	v_cndmask_b32_e64 v41, v41, v190, s[24:25]
	v_cndmask_b32_e64 v58, v58, v190, s[26:27]
	v_cndmask_b32_e64 v42, v42, v190, s[28:29]
	v_cndmask_b32_e64 v59, v59, v190, s[30:31]
	v_cndmask_b32_e64 v43, v43, v190, s[34:35]
	v_cndmask_b32_e64 v60, v60, v190, s[36:37]
	v_cndmask_b32_e64 v44, v44, v190, s[38:39]
	v_cndmask_b32_e64 v61, v61, v190, s[40:41]
	v_cndmask_b32_e64 v45, v45, v190, s[42:43]
	v_cndmask_b32_e64 v62, v62, v190, s[44:45]
	v_cndmask_b32_e64 v46, v46, v190, s[46:47]
	v_cndmask_b32_e64 v63, v63, v190, s[48:49]
	v_cndmask_b32_e64 v47, v47, v190, s[50:51]
	v_cndmask_b32_e64 v64, v64, v190, s[52:53]
	v_cndmask_b32_e64 v48, v48, v190, s[54:55]
	v_cndmask_b32_e64 v65, v65, v190, s[56:57]
	v_cndmask_b32_e64 v49, v49, v190, s[58:59]
	v_cndmask_b32_e64 v66, v66, v190, s[60:61]
	v_cndmask_b32_e64 v50, v50, v190, s[62:63]
	v_cndmask_b32_e64 v67, v67, v190, s[64:65]
	v_cndmask_b32_e64 v51, v51, v190, s[66:67]
.LBB2_5:
	s_or_b64 exec, exec, s[74:75]
	s_nop 8
	v_max3_f32 v34, v52, v53, v54
	v_max3_f32 v192, v36, v37, v38
	v_max3_f32 v34, v34, v55, v56
	v_max3_f32 v192, v192, v39, v40
	v_max3_f32 v34, v34, v57, v58
	v_max3_f32 v192, v192, v41, v42
	v_max3_f32 v34, v34, v59, v60
	v_max3_f32 v192, v192, v43, v44
	v_max3_f32 v34, v34, v61, v62
	v_max3_f32 v192, v192, v45, v46
	v_max3_f32 v34, v34, v63, v64
	v_max3_f32 v192, v192, v47, v48
	v_max3_f32 v34, v34, v65, v66
	v_max3_f32 v192, v192, v49, v50
	v_max3_f32 v193, v34, v192, v67
	v_max_f32_e32 v193, v193, v51
	v_mov_b32_e32 v194, v193
	v_mov_b32_e32 v192, v193
	s_nop 1
	v_permlane32_swap_b32_e32 v194, v192
	v_max3_f32 v193, v193, v194, v192
	v_add_f32_e32 v194, 0x41000000, v189
	v_cmp_gt_f32_e32 vcc, v193, v194
	s_cbranch_vccz .LBB2_2
	v_max_f32_e32 v193, v193, v193
	v_max_f32_e32 v194, v189, v189
	v_max_f32_e32 v193, v194, v193
	v_sub_f32_e32 v189, v189, v193
	v_exp_f32_e32 v194, v189
	v_mov_b32_e32 v189, v193
	v_pk_mul_f32 v[32:33], v[194:195], v[32:33] op_sel_hi:[0,1]
	v_pk_mul_f32 v[30:31], v[194:195], v[30:31] op_sel_hi:[0,1]
	v_pk_mul_f32 v[28:29], v[194:195], v[28:29] op_sel_hi:[0,1]
	v_pk_mul_f32 v[26:27], v[194:195], v[26:27] op_sel_hi:[0,1]
	v_pk_mul_f32 v[24:25], v[194:195], v[24:25] op_sel_hi:[0,1]
	v_pk_mul_f32 v[22:23], v[194:195], v[22:23] op_sel_hi:[0,1]
	v_pk_mul_f32 v[20:21], v[194:195], v[20:21] op_sel_hi:[0,1]
	v_pk_mul_f32 v[18:19], v[194:195], v[18:19] op_sel_hi:[0,1]
	v_pk_mul_f32 v[16:17], v[194:195], v[16:17] op_sel_hi:[0,1]
	v_pk_mul_f32 v[14:15], v[194:195], v[14:15] op_sel_hi:[0,1]
	v_pk_mul_f32 v[12:13], v[194:195], v[12:13] op_sel_hi:[0,1]
	v_pk_mul_f32 v[10:11], v[194:195], v[10:11] op_sel_hi:[0,1]
	v_pk_mul_f32 v[8:9], v[194:195], v[8:9] op_sel_hi:[0,1]
	v_pk_mul_f32 v[6:7], v[194:195], v[6:7] op_sel_hi:[0,1]
	v_pk_mul_f32 v[4:5], v[194:195], v[4:5] op_sel_hi:[0,1]
	v_pk_mul_f32 v[2:3], v[194:195], v[2:3] op_sel_hi:[0,1]
	v_mul_f32_e32 v187, v187, v194
	s_branch .LBB2_2
.LBB2_7:
	s_or_b64 exec, exec, s[72:73]
	v_and_b32_e32 v192, 64, v188
	v_xor_b32_e32 v34, 32, v188
	v_add_u32_e32 v192, 64, v192

	.amdhsa_kernel _Z11attn_kernelPK14__hip_bfloat16S1_S1_PS_
		.amdhsa_group_segment_fixed_size 35840
		.amdhsa_private_segment_fixed_size 0
		.amdhsa_kernarg_size 32
		.amdhsa_user_sgpr_count 2
		.amdhsa_user_sgpr_dispatch_ptr 0
		.amdhsa_user_sgpr_queue_ptr 0
		.amdhsa_user_sgpr_kernarg_segment_ptr 1
		.amdhsa_user_sgpr_dispatch_id 0
		.amdhsa_user_sgpr_kernarg_preload_length 0
		.amdhsa_user_sgpr_kernarg_preload_offset 0
		.amdhsa_user_sgpr_private_segment_size 0
		.amdhsa_uses_dynamic_stack 0
		.amdhsa_enable_private_segment 0
		.amdhsa_system_sgpr_workgroup_id_x 1
		.amdhsa_system_sgpr_workgroup_id_y 0
		.amdhsa_system_sgpr_workgroup_id_z 0
		.amdhsa_system_sgpr_workgroup_info 0
		.amdhsa_system_vgpr_workitem_id 0
		.amdhsa_next_free_vgpr 204
		.amdhsa_next_free_sgpr 96
		.amdhsa_accum_offset 204
		.amdhsa_reserve_vcc 1
		.amdhsa_float_round_mode_32 0
		.amdhsa_float_round_mode_16_64 0
		.amdhsa_float_denorm_mode_32 3
		.amdhsa_float_denorm_mode_16_64 3
		.amdhsa_dx10_clamp 1
		.amdhsa_ieee_mode 1
		.amdhsa_fp16_overflow 0
		.amdhsa_tg_split 0
		.amdhsa_exception_fp_ieee_invalid_op 0
		.amdhsa_exception_fp_denorm_src 0
		.amdhsa_exception_fp_ieee_div_zero 0
		.amdhsa_exception_fp_ieee_overflow 0
		.amdhsa_exception_fp_ieee_underflow 0
		.amdhsa_exception_fp_ieee_inexact 0
		.amdhsa_exception_int_div_zero 0
	.end_amdhsa_kernel

amdhsa.kernels:
  - .agpr_count:     0
    .args:
      - .actual_access:  read_only
        .address_space:  global
        .offset:         0
        .size:           8
        .value_kind:     global_buffer
      - .actual_access:  read_only
        .address_space:  global
        .offset:         8
        .size:           8
        .value_kind:     global_buffer
      - .actual_access:  read_only
        .address_space:  global
        .offset:         16
        .size:           8
        .value_kind:     global_buffer
      - .actual_access:  read_only
        .address_space:  global
        .offset:         24
        .size:           8
        .value_kind:     global_buffer
      - .actual_access:  read_only
        .address_space:  global
        .offset:         32
        .size:           8
        .value_kind:     global_buffer
      - .actual_access:  read_only
        .address_space:  global
        .offset:         40
        .size:           8
        .value_kind:     global_buffer
      - .actual_access:  read_only
        .address_space:  global
        .offset:         48
        .size:           8
        .value_kind:     global_buffer
      - .actual_access:  write_only
        .address_space:  global
        .offset:         56
        .size:           8
        .value_kind:     global_buffer
      - .actual_access:  write_only
        .address_space:  global
        .offset:         64
        .size:           8
        .value_kind:     global_buffer
      - .actual_access:  write_only
        .address_space:  global
        .offset:         72
        .size:           8
        .value_kind:     global_buffer
    .group_segment_fixed_size: 0
    .kernarg_segment_align: 8
    .kernarg_segment_size: 80
    .language:       OpenCL C
    .language_version:
      - 2
      - 0
    .max_flat_workgroup_size: 256
    .name:           _Z11prep_kernelPKfS0_S0_S0_S0_S0_S0_PcS1_S1_
    .private_segment_fixed_size: 0
    .sgpr_count:     21
    .sgpr_spill_count: 0
    .symbol:         _Z11prep_kernelPKfS0_S0_S0_S0_S0_S0_PcS1_S1_.kd
    .uniform_work_group_size: 1
    .uses_dynamic_stack: false
    .vgpr_count:     52
    .vgpr_spill_count: 0
    .wavefront_size: 64
  - .agpr_count:     0
    .args:
      - .address_space:  global
        .offset:         0
        .size:           8
        .value_kind:     global_buffer
      - .address_space:  global
        .offset:         8
        .size:           8
        .value_kind:     global_buffer
      - .actual_access:  read_only
        .address_space:  global
        .offset:         16
        .size:           8
        .value_kind:     global_buffer
      - .actual_access:  read_only
        .address_space:  global
        .offset:         24
        .size:           8
        .value_kind:     global_buffer
      - .actual_access:  read_only
        .address_space:  global
        .offset:         32
        .size:           8
        .value_kind:     global_buffer
      - .actual_access:  write_only
        .address_space:  global
        .offset:         40
        .size:           8
        .value_kind:     global_buffer
      - .actual_access:  write_only
        .address_space:  global
        .offset:         48
        .size:           8
        .value_kind:     global_buffer
      - .actual_access:  write_only
        .address_space:  global
        .offset:         56
        .size:           8
        .value_kind:     global_buffer
      - .actual_access:  read_only
        .address_space:  global
        .offset:         64
        .size:           8
        .value_kind:     global_buffer
      - .actual_access:  write_only
        .address_space:  global
        .offset:         72
        .size:           8
        .value_kind:     global_buffer
    .group_segment_fixed_size: 131072
    .kernarg_segment_align: 8
    .kernarg_segment_size: 80
    .language:       OpenCL C
    .language_version:
      - 2
      - 0
    .max_flat_workgroup_size: 768
    .name:           _Z8qkv_gemmPKcS0_PKfS2_S2_P14__hip_bfloat16S4_S4_S2_Pc
    .private_segment_fixed_size: 0
    .sgpr_count:     106
    .sgpr_spill_count: 2
    .symbol:         _Z8qkv_gemmPKcS0_PKfS2_S2_P14__hip_bfloat16S4_S4_S2_Pc.kd
    .uniform_work_group_size: 1
    .uses_dynamic_stack: false
    .vgpr_count:     85
    .vgpr_spill_count: 0
    .wavefront_size: 64
  - .agpr_count:     0
    .args:
      - .address_space:  global
        .offset:         0
        .size:           8
        .value_kind:     global_buffer
      - .address_space:  global
        .offset:         8
        .size:           8
        .value_kind:     global_buffer
      - .address_space:  global
        .offset:         16
        .size:           8
        .value_kind:     global_buffer
      - .actual_access:  write_only
        .address_space:  global
        .offset:         24
        .size:           8
        .value_kind:     global_buffer
    .group_segment_fixed_size: 35840
    .kernarg_segment_align: 8
    .kernarg_segment_size: 32
    .language:       OpenCL C
    .language_version:
      - 2
      - 0
    .max_flat_workgroup_size: 256
    .name:           _Z11attn_kernelPK14__hip_bfloat16S1_S1_PS_
    .private_segment_fixed_size: 0
    .sgpr_count:     84
    .sgpr_spill_count: 0
    .symbol:         _Z11attn_kernelPK14__hip_bfloat16S1_S1_PS_.kd
    .uniform_work_group_size: 1
    .uses_dynamic_stack: false
    .vgpr_count:     204
    .vgpr_spill_count: 0
    .wavefront_size: 64
  - .agpr_count:     0
    .args:
      - .address_space:  global
        .offset:         0
        .size:           8
        .value_kind:     global_buffer
      - .address_space:  global
        .offset:         8
        .size:           8
        .value_kind:     global_buffer
      - .actual_access:  read_only
        .address_space:  global
        .offset:         16
        .size:           8
        .value_kind:     global_buffer
      - .actual_access:  read_only
        .address_space:  global
        .offset:         24
        .size:           8
        .value_kind:     global_buffer
      - .actual_access:  write_only
        .address_space:  global
        .offset:         32
        .size:           8
        .value_kind:     global_buffer
    .group_segment_fixed_size: 147456
    .kernarg_segment_align: 8
    .kernarg_segment_size: 40
    .language:       OpenCL C
    .language_version:
      - 2
      - 0
    .max_flat_workgroup_size: 512
    .name:           _Z7fc_gemmPKcS0_PKfS2_Pf
    .private_segment_fixed_size: 0
    .sgpr_count:     21
    .sgpr_spill_count: 0
    .symbol:         _Z7fc_gemmPKcS0_PKfS2_Pf.kd
    .uniform_work_group_size: 1
    .uses_dynamic_stack: false
    .vgpr_count:     192
    .vgpr_spill_count: 0
    .wavefront_size: 64
  - .agpr_count:     0
    .args:
      - .actual_access:  read_only
        .address_space:  global
        .offset:         0
        .size:           8
        .value_kind:     global_buffer
      - .actual_access:  write_only
        .address_space:  global
        .offset:         8
        .size:           8
        .value_kind:     global_buffer
      - .actual_access:  read_only
        .address_space:  global
        .offset:         16
        .size:           8
        .value_kind:     global_buffer
      - .actual_access:  read_only
        .address_space:  global
        .offset:         24
        .size:           8
        .value_kind:     global_buffer
    .group_segment_fixed_size: 16
    .kernarg_segment_align: 8
    .kernarg_segment_size: 32
    .language:       OpenCL C
    .language_version:
      - 2
      - 0
    .max_flat_workgroup_size: 256
    .name:           _Z9ln_kernelPKfPfS0_S0_
    .private_segment_fixed_size: 0
    .sgpr_count:     18
    .sgpr_spill_count: 0
    .symbol:         _Z9ln_kernelPKfPfS0_S0_.kd
    .uniform_work_group_size: 1
    .uses_dynamic_stack: false
    .vgpr_count:     74
    .vgpr_spill_count: 0
    .wavefront_size: 64
  - .agpr_count:     0
    .args:           []
    .group_segment_fixed_size: 0
    .kernarg_segment_align: 4
    .kernarg_segment_size: 0
    .language:       OpenCL C
    .language_version:
      - 2
      - 0
    .max_flat_workgroup_size: 1024
    .name:           _Z12empty_kernelv
    .private_segment_fixed_size: 0
    .sgpr_count:     6
    .sgpr_spill_count: 0
    .symbol:         _Z12empty_kernelv.kd
    .uniform_work_group_size: 1
    .uses_dynamic_stack: false
    .vgpr_count:     0
    .vgpr_spill_count: 0
    .wavefront_size: 64
